# u14 + conversion read-back and stores moved behind the mid-iteration barrier (LDS round trip overlaps the barrier)
# baseline (speedup 1.0000x reference)
; #define VM0() asm volatile("s_waitcnt vmcnt(0)" ::: "memory")
; DEVI void cv_finish(char* img  , int lane, const CvRegs& R) {
;     ...
;     const int n = lane >> 1, half = lane & 1; u32x4 w0, w1;
; #pragma unroll
;     for (int j = 0; j < 4; ++j) { w0[j] = *(const unsigned*)(img + n * 68 + half * 32 + j * 4); w1[j] = *(const unsigned*)(img + n * 68 + half * 32 + 16 + j * 4); }
;     const int row = R.c.perm ? R.c.r0 + 128 * ((n >> 3) & 1) + 16 * ((n >> 2) & 1) + 4 * (n >> 4) + (n & 3) : R.c.r0 + 128 * ((n >> 2) & 1) + 4 * (n >> 3) + (n & 3);
;     bf16_t* d = R.c.dst + (size_t)row * R.c.K + R.c.k0 + half * 16;
;     __builtin_nontemporal_store(w0, (u32x4*)d); __builtin_nontemporal_store(w1, (u32x4*)(d + 8));
;     asm volatile("" ::: "memory"); __builtin_amdgcn_wave_barrier();
; DEVI void attn_unit8(const Params& p, char* smem, int unit, int l, int& cvs  , CvRun& crun) {
;     ...
;         if (cvr.live) asm volatile("s_waitcnt vmcnt(2)" ::: "memory"); else VM0();
;         __syncthreads();
;         if (T + 2 < NTILE) B_DMA(T + 2, s2);
;         qkt(pA0, pA1, K_lds + s1 * 24576, qr, r32, hi, cinit);
.LBB0_702:
	s_mul_i32 s98, s2, 0x6000
	s_add_i32 s98, s96, s98
	s_lshl_b32 s99, s2, 14
	s_add_i32 s99, s97, s99
	s_mul_i32 s6, s61, 0x6000
	s_add_i32 s6, s6, 0
	v_add_u32_e32 v249, s6, v129
	v_lshl_add_u64 v[250:251], v[118:119], 0, s[12:13]
	s_mov_b32 m0, s98
	s_barrier
	ds_read_b128 v[234:237], v249
	ds_read_b128 v[210:213], v249 offset:6144
	global_load_lds_dwordx4 v[250:251], off
	s_cmp_lg_u64 s[14:15], 0
	s_cbranch_scc0 .Lmy_cvp2_a
	ds_read2_b32 v[66:67], v68 offset1:1
	ds_read2_b32 v[70:71], v68 offset0:4 offset1:5
	ds_read2_b32 v[72:73], v68 offset0:6 offset1:7
	ds_read2_b32 v[68:69], v68 offset0:2 offset1:3
	v_add_u32_e32 v74, s8, v74
	v_mad_i64_i32 v[74:75], s[100:101], v74, s94, 0
	v_lshl_add_u64 v[74:75], v[74:75], 1, v[172:173]
	s_ashr_i32 s11, s10, 31
	v_lshl_add_u64 v[74:75], s[10:11], 1, v[74:75]
	v_lshlrev_b32_e32 v174, 1, v180
	v_lshl_add_u64 v[74:75], v[74:75], 0, v[174:175]
	s_waitcnt lgkmcnt(0)
	global_store_dwordx4 v[74:75], v[66:69], off nt
	global_store_dwordx4 v[74:75], v[70:73], off offset:16 nt
; template <bool FIRST> DEVI bool partialSM(f32x16& p0, f32x16& p1, float& m_reg, float& alpha) {
;     float pmax = p0[0];
; #pragma unroll
;     for (int r = 1; r < 16; ++r) pmax = fmaxf(pmax, p0[r]);
; #pragma unroll
;     for (int r = 0; r < 16; ++r) pmax = fmaxf(pmax, p1[r]);
;     { auto rr = __builtin_amdgcn_permlane32_swap(__float_as_uint(pmax), __float_as_uint(pmax), false, false);
;       pmax = fmaxf(__uint_as_float(rr[0]), __uint_as_float(rr[1])); }
;     if (FIRST) { m_reg = pmax; alpha = 1.f;
; #pragma unroll
;         for (int r = 0; r < 16; ++r) { p0[r] = __builtin_amdgcn_exp2f(p0[r] - pmax); p1[r] = p1[r] - pmax; }
;         return false;
;     } else if (__builtin_expect(__all(pmax <= ATT_THR), 1)) { alpha = 1.f;
; #pragma unroll
;         for (int r = 0; r < 16; ++r) p0[r] = __builtin_amdgcn_exp2f(p0[r]);
;         return false;
;     } else { const float d = fmaxf(pmax, 0.f); alpha = __builtin_amdgcn_exp2f(-d); m_reg += d;
; #pragma unroll
;         for (int r = 0; r < 16; ++r) { p0[r] = __builtin_amdgcn_exp2f(p0[r] - d); p1[r] = p1[r] - d; }
;         return true;
;     }
; }
; DEVI void finishSM(f32x16& p0, f32x16& p1, float alpha, float& l_reg, bf16x8& pa0, bf16x8& pa1, bf16x8& pa2, bf16x8& pa3) {
; #pragma unroll
;     for (int r = 0; r < 16; ++r) p1[r] = __builtin_amdgcn_exp2f(p1[r]);
;     f32x2 s2 = (f32x2){p0[0], p0[1]} + (f32x2){p1[0], p1[1]};
; #pragma unroll
;     for (int r = 2; r < 16; r += 2) s2 += (f32x2){p0[r], p0[r + 1]} + (f32x2){p1[r], p1[r + 1]};
;     float ps = s2[0] + s2[1];
;     { auto rr = __builtin_amdgcn_permlane32_swap(__float_as_uint(ps), __float_as_uint(ps), false, false);
;       ps = __uint_as_float(rr[0]) + __uint_as_float(rr[1]); }
;     l_reg = l_reg * alpha + ps;
;     ...
;     PK4(p0, 0, pa0); PK4(p0, 8, pa1); PK4(p1, 0, pa2); PK4(p1, 8, pa3);
;     ...
; }
; DEVI void qkt(f32x16& p0, f32x16& p1, const char* Kb, const bf16x8 (&qr)[6], int r32, int hi, const f32x16& cinit) {
; #pragma unroll
;     for (int d0 = 0; d0 < 6; ++d0) { const int cb = (d0 * 16 + hi * 8) * 2;
;         const bf16x8 k0 = *(const bf16x8*)(Kb + KSWZ(r32, cb)), k1 = *(const bf16x8*)(Kb + KSWZ(32 + r32, cb));
;         p0 = __builtin_amdgcn_mfma_f32_32x32x16_bf16(k0, qr[d0], d0 == 0 ? cinit : p0, 0, 0, 0);
;         p1 = __builtin_amdgcn_mfma_f32_32x32x16_bf16(k1, qr[d0], d0 == 0 ? cinit : p1, 0, 0, 0); }
; }
.Lmy_cvp2_a:
	v_exp_f32_e32 v82, v82
	s_waitcnt lgkmcnt(1)
	v_mfma_f32_32x32x16_bf16 v[98:113], v[234:237], v[150:153], v[34:49]
	v_add_u32_e32 v126, s6, v184
	v_lshl_add_u64 v[250:251], v[120:121], 0, s[12:13]
	s_add_i32 m0, s98, 0x2000
	v_exp_f32_e32 v83, v83
	v_exp_f32_e32 v84, v84
	global_load_lds_dwordx4 v[250:251], off
	v_exp_f32_e32 v85, v85
	v_exp_f32_e32 v86, v86
	v_exp_f32_e32 v87, v87
	v_exp_f32_e32 v88, v88
	s_waitcnt lgkmcnt(0)
	v_mfma_f32_32x32x16_bf16 v[66:81], v[210:213], v[150:153], v[34:49]
	ds_read_b128 v[210:213], v126
	ds_read_b128 v[214:217], v126 offset:6144
	v_add_u32_e32 v126, s6, v185
	v_lshl_add_u64 v[250:251], v[122:123], 0, s[12:13]
	s_add_i32 m0, s98, 0x4000
	v_exp_f32_e32 v89, v89
	v_exp_f32_e32 v90, v90
	global_load_lds_dwordx4 v[250:251], off
	v_exp_f32_e32 v91, v91
	v_exp_f32_e32 v92, v92
	v_exp_f32_e32 v93, v93
	s_waitcnt lgkmcnt(1)
	v_mfma_f32_32x32x16_bf16 v[98:113], v[210:213], v[138:141], v[98:113]
	s_mov_b32 m0, s99
	v_exp_f32_e32 v94, v94
	v_exp_f32_e32 v95, v95
	v_lshl_add_u64 v[250:251], v[116:117], 0, s[40:41]
	global_load_lds_dwordx4 v[116:117], off
	s_add_i32 m0, s99, 0x2000
	v_exp_f32_e32 v96, v96
	v_exp_f32_e32 v97, v97
	v_add_u32_e32 v174, 0x2000, v202
	global_load_lds_dwordx4 v[250:251], off
	s_waitcnt lgkmcnt(0)
	v_mfma_f32_32x32x16_bf16 v[66:81], v[214:217], v[138:141], v[66:81]
	ds_read_b128 v[210:213], v126
	ds_read_b128 v[214:217], v126 offset:6144
	v_add_u32_e32 v126, s6, v204
	s_waitcnt lgkmcnt(1)
	v_mfma_f32_32x32x16_bf16 v[98:113], v[210:213], v[134:137], v[98:113]
	ds_read_b128 v[210:213], v126
	ds_read_b128 v[218:221], v126 offset:6144
	v_add_u32_e32 v126, s6, v205
	s_waitcnt lgkmcnt(2)
	v_mfma_f32_32x32x16_bf16 v[66:81], v[214:217], v[134:137], v[66:81]
	ds_read_b128 v[214:217], v126
	ds_read_b128 v[222:225], v126 offset:6144
	v_add_u32_e32 v126, s6, v206
	ds_read_b128 v[226:229], v126
	ds_read_b128 v[230:233], v126 offset:6144
	v_add_f32_e32 v126, v50, v82
	v_add_f32_e32 v127, v51, v83
	v_cvt_pk_bf16_f32 v50, v50, v51
	v_cvt_pk_bf16_f32 v51, v52, v53
	s_waitcnt lgkmcnt(5)
	v_mfma_f32_32x32x16_bf16 v[98:113], v[210:213], v[130:133], v[98:113]
	v_add_f32_e64 v210, v52, v84
	v_add_f32_e64 v211, v53, v85
	v_cvt_pk_bf16_f32 v52, v54, v55
	v_cvt_pk_bf16_f32 v53, v56, v57
	v_add_f32_e64 v126, v210, v126
	v_add_f32_e64 v127, v211, v127
	v_add_f32_e64 v210, v54, v86
	v_add_f32_e64 v211, v55, v87
	v_cvt_pk_bf16_f32 v54, v58, v59
	s_waitcnt lgkmcnt(4)
	v_mfma_f32_32x32x16_bf16 v[66:81], v[218:221], v[130:133], v[66:81]
	v_add_f32_e64 v126, v210, v126
	v_add_f32_e64 v127, v211, v127
	v_add_f32_e64 v210, v56, v88
	v_add_f32_e64 v211, v57, v89
	v_cvt_pk_bf16_f32 v55, v60, v61
	v_cvt_pk_bf16_f32 v56, v62, v63
	v_cvt_pk_bf16_f32 v57, v64, v65
	v_add_f32_e64 v126, v210, v126
	v_add_f32_e64 v127, v211, v127
	v_add_f32_e32 v210, v58, v90
	v_add_f32_e32 v211, v59, v91
	v_cvt_pk_bf16_f32 v58, v82, v83
	v_cvt_pk_bf16_f32 v59, v84, v85
	s_waitcnt lgkmcnt(3)
	v_mfma_f32_32x32x16_bf16 v[98:113], v[214:217], v[146:149], v[98:113]
	v_add_f32_e64 v126, v210, v126
	v_add_f32_e64 v127, v211, v127
	v_add_f32_e64 v210, v60, v92
	v_add_f32_e64 v211, v61, v93
	v_cvt_pk_bf16_f32 v60, v86, v87
	v_cvt_pk_bf16_f32 v61, v88, v89
	v_add_f32_e64 v126, v210, v126
	v_add_f32_e64 v127, v211, v127
	v_add_f32_e32 v210, v62, v94
	v_add_f32_e32 v211, v63, v95
	v_cvt_pk_bf16_f32 v62, v90, v91
	v_cvt_pk_bf16_f32 v63, v92, v93
	s_waitcnt lgkmcnt(2)
	v_mfma_f32_32x32x16_bf16 v[66:81], v[222:225], v[146:149], v[66:81]
	v_add_f32_e64 v126, v210, v126
	v_add_f32_e64 v127, v211, v127
	v_add_f32_e64 v210, v64, v96
	v_add_f32_e64 v211, v65, v97
	v_cvt_pk_bf16_f32 v64, v94, v95
	v_cvt_pk_bf16_f32 v65, v96, v97
	ds_read_b64_tr_b16 v[154:155], v174 offset:0
	ds_read_b64_tr_b16 v[156:157], v174 offset:0x400
	ds_read_b64_tr_b16 v[158:159], v174 offset:0x800
	ds_read_b64_tr_b16 v[160:161], v174 offset:0xc00
	ds_read_b64_tr_b16 v[162:163], v174 offset:0x1000
	ds_read_b64_tr_b16 v[164:165], v174 offset:0x1400
	ds_read_b64_tr_b16 v[166:167], v174 offset:0x1800
	ds_read_b64_tr_b16 v[168:169], v174 offset:0x1c00
	v_add_f32_e64 v126, v210, v126
	v_add_f32_e64 v127, v211, v127
	ds_read_b64_tr_b16 v[210:211], v174 offset:0x200
	ds_read_b64_tr_b16 v[212:213], v174 offset:0x600
	ds_read_b64_tr_b16 v[214:215], v174 offset:0xa00
	s_waitcnt lgkmcnt(12)
	v_mfma_f32_32x32x16_bf16 v[98:113], v[226:229], v[142:145], v[98:113]
	ds_read_b64_tr_b16 v[216:217], v174 offset:0xe00
	ds_read_b64_tr_b16 v[218:219], v174 offset:0x1200
	ds_read_b64_tr_b16 v[220:221], v174 offset:0x1600
	ds_read_b64_tr_b16 v[222:223], v174 offset:0x1a00
	ds_read_b64_tr_b16 v[224:225], v174 offset:0x1e00
	v_add_f32_e32 v126, v126, v127
	s_waitcnt lgkmcnt(15)
	v_mfma_f32_32x32x16_bf16 v[66:81], v[230:233], v[142:145], v[66:81]
	v_mov_b32_e32 v127, v126
	s_nop 1
	v_permlane32_swap_b32_e32 v126, v127
	s_waitcnt lgkmcnt(14)
	v_mfma_f32_32x32x16_bf16 v[18:33], v[50:53], v[154:157], v[18:33]
	s_waitcnt lgkmcnt(6)
	v_mfma_f32_32x32x16_bf16 v[2:17], v[50:53], v[210:213], v[2:17]
	s_nop 4
	v_max_f32_e32 v249, v99, v99
	v_max_f32_e32 v250, v98, v98
	v_max_f32_e32 v249, v250, v249
	v_max3_f32 v249, v249, v100, v101
	v_max3_f32 v249, v249, v102, v103
	v_max3_f32 v251, v249, v104, v105
	v_max3_f32 v251, v251, v106, v107
	v_exp_f32_e32 v50, v98
	v_exp_f32_e32 v51, v99
	v_exp_f32_e32 v52, v100
	v_exp_f32_e32 v53, v101
	v_mfma_f32_32x32x16_bf16 v[18:33], v[54:57], v[158:161], v[18:33]
	s_waitcnt lgkmcnt(4)
	v_mfma_f32_32x32x16_bf16 v[2:17], v[54:57], v[214:217], v[2:17]
	v_max3_f32 v251, v251, v108, v109
	v_max3_f32 v251, v251, v110, v111
	v_max3_f32 v251, v251, v112, v113
	v_max3_f32 v251, v251, v66, v67
	v_max3_f32 v251, v251, v68, v69
	v_max3_f32 v251, v251, v70, v71
	v_max3_f32 v251, v251, v72, v73
	v_exp_f32_e32 v54, v102
	v_exp_f32_e32 v55, v103
	v_exp_f32_e32 v56, v104
	v_exp_f32_e32 v57, v105
	v_mfma_f32_32x32x16_bf16 v[18:33], v[58:61], v[162:165], v[18:33]
	s_waitcnt lgkmcnt(2)
	v_mfma_f32_32x32x16_bf16 v[2:17], v[58:61], v[218:221], v[2:17]
	v_max3_f32 v251, v251, v74, v75
	v_max3_f32 v251, v251, v76, v77
	v_max3_f32 v251, v251, v78, v79
	v_max3_f32 v251, v251, v80, v81
	v_mov_b32_e32 v252, v251
	s_nop 1
	v_permlane32_swap_b32_e32 v251, v252
	v_exp_f32_e32 v58, v106
	v_exp_f32_e32 v59, v107
	v_exp_f32_e32 v60, v108
	v_exp_f32_e32 v61, v109
	v_mfma_f32_32x32x16_bf16 v[18:33], v[62:65], v[166:169], v[18:33]
	s_waitcnt lgkmcnt(0)
	v_mfma_f32_32x32x16_bf16 v[2:17], v[62:65], v[222:225], v[2:17]
	v_exp_f32_e32 v62, v110
	v_exp_f32_e32 v63, v111
	v_exp_f32_e32 v64, v112
	v_exp_f32_e32 v65, v113
	v_max_f32_e32 v252, v252, v252
	v_max_f32_e32 v251, v251, v251
	v_max_f32_e32 v174, v251, v252
	v_cmp_ge_f32_e32 vcc, s79, v174
	s_cmp_lg_u64 vcc, exec
	s_cselect_b64 s[6:7], -1, 0
	s_cbranch_scc1 .LBB0_711
	v_mov_b32_e32 v202, 1.0
	v_mov_b32_e32 v203, v209
	s_branch .LBB0_716

; #define VM0() asm volatile("s_waitcnt vmcnt(0)" ::: "memory")
; DEVI void attn_unit8(const Params& p, char* smem, int unit, int l, int& cvs  , CvRun& crun) {
;     ...
;         cv_finish(smem + 124928 + wid * 2304, lane, cvr);
;         if (cvr.live) asm volatile("s_waitcnt vmcnt(2)" ::: "memory"); else VM0();
;         __syncthreads();
.Lmy_cvj_a:
	s_branch .LBB0_702

; #define VM0() asm volatile("s_waitcnt vmcnt(0)" ::: "memory")
; DEVI void cv_finish(char* img  , int lane, const CvRegs& R) {
;     ...
;     const int n = lane >> 1, half = lane & 1; u32x4 w0, w1;
; #pragma unroll
;     for (int j = 0; j < 4; ++j) { w0[j] = *(const unsigned*)(img + n * 68 + half * 32 + j * 4); w1[j] = *(const unsigned*)(img + n * 68 + half * 32 + 16 + j * 4); }
;     const int row = R.c.perm ? R.c.r0 + 128 * ((n >> 3) & 1) + 16 * ((n >> 2) & 1) + 4 * (n >> 4) + (n & 3) : R.c.r0 + 128 * ((n >> 2) & 1) + 4 * (n >> 3) + (n & 3);
;     bf16_t* d = R.c.dst + (size_t)row * R.c.K + R.c.k0 + half * 16;
;     __builtin_nontemporal_store(w0, (u32x4*)d); __builtin_nontemporal_store(w1, (u32x4*)(d + 8));
;     asm volatile("" ::: "memory"); __builtin_amdgcn_wave_barrier();
; DEVI void attn_unit8(const Params& p, char* smem, int unit, int l, int& cvs  , CvRun& crun) {
;     ...
;         if (cvr.live) asm volatile("s_waitcnt vmcnt(2)" ::: "memory"); else VM0();
;         __syncthreads();
;         if (T + 2 < NTILE) B_DMA(T + 2, s2);
;         qkt(pA0, pA1, K_lds + s1 * 24576, qr, r32, hi, cinit);
.LBB0_2266:
	s_mul_i32 s98, s61, 0x6000
	s_add_i32 s98, s96, s98
	s_lshl_b32 s99, s61, 14
	s_add_i32 s99, s97, s99
	s_mul_i32 s6, s2, 0x6000
	s_add_i32 s6, s6, 0
	v_add_u32_e32 v249, s6, v129
	v_lshl_add_u64 v[250:251], v[118:119], 0, s[12:13]
	s_mov_b32 m0, s98
	s_barrier
	ds_read_b128 v[234:237], v249
	ds_read_b128 v[212:215], v249 offset:6144
	global_load_lds_dwordx4 v[250:251], off
	s_cmp_lg_u64 s[14:15], 0
	s_cbranch_scc0 .Lmy_cvp2_b
	ds_read2_b32 v[66:67], v68 offset1:1
	ds_read2_b32 v[70:71], v68 offset0:4 offset1:5
	ds_read2_b32 v[72:73], v68 offset0:6 offset1:7
	ds_read2_b32 v[68:69], v68 offset0:2 offset1:3
	v_add_u32_e32 v74, s8, v74
	v_mad_i64_i32 v[74:75], s[100:101], v74, s94, 0
	v_lshl_add_u64 v[74:75], v[74:75], 1, v[172:173]
	s_ashr_i32 s11, s10, 31
	v_lshl_add_u64 v[74:75], s[10:11], 1, v[74:75]
	v_lshlrev_b32_e32 v174, 1, v180
	v_lshl_add_u64 v[74:75], v[74:75], 0, v[174:175]
	s_waitcnt lgkmcnt(0)
	global_store_dwordx4 v[74:75], v[66:69], off nt
	global_store_dwordx4 v[74:75], v[70:73], off offset:16 nt
; template <bool FIRST> DEVI bool partialSM(f32x16& p0, f32x16& p1, float& m_reg, float& alpha) {
;     float pmax = p0[0];
; #pragma unroll
;     for (int r = 1; r < 16; ++r) pmax = fmaxf(pmax, p0[r]);
; #pragma unroll
;     for (int r = 0; r < 16; ++r) pmax = fmaxf(pmax, p1[r]);
;     { auto rr = __builtin_amdgcn_permlane32_swap(__float_as_uint(pmax), __float_as_uint(pmax), false, false);
;       pmax = fmaxf(__uint_as_float(rr[0]), __uint_as_float(rr[1])); }
;     if (FIRST) { m_reg = pmax; alpha = 1.f;
; #pragma unroll
;         for (int r = 0; r < 16; ++r) { p0[r] = __builtin_amdgcn_exp2f(p0[r] - pmax); p1[r] = p1[r] - pmax; }
;         return false;
;     } else if (__builtin_expect(__all(pmax <= ATT_THR), 1)) { alpha = 1.f;
; #pragma unroll
;         for (int r = 0; r < 16; ++r) p0[r] = __builtin_amdgcn_exp2f(p0[r]);
;         return false;
;     } else { const float d = fmaxf(pmax, 0.f); alpha = __builtin_amdgcn_exp2f(-d); m_reg += d;
; #pragma unroll
;         for (int r = 0; r < 16; ++r) { p0[r] = __builtin_amdgcn_exp2f(p0[r] - d); p1[r] = p1[r] - d; }
;         return true;
;     }
; }
; DEVI void finishSM(f32x16& p0, f32x16& p1, float alpha, float& l_reg, bf16x8& pa0, bf16x8& pa1, bf16x8& pa2, bf16x8& pa3) {
; #pragma unroll
;     for (int r = 0; r < 16; ++r) p1[r] = __builtin_amdgcn_exp2f(p1[r]);
;     f32x2 s2 = (f32x2){p0[0], p0[1]} + (f32x2){p1[0], p1[1]};
; #pragma unroll
;     for (int r = 2; r < 16; r += 2) s2 += (f32x2){p0[r], p0[r + 1]} + (f32x2){p1[r], p1[r + 1]};
;     float ps = s2[0] + s2[1];
;     { auto rr = __builtin_amdgcn_permlane32_swap(__float_as_uint(ps), __float_as_uint(ps), false, false);
;       ps = __uint_as_float(rr[0]) + __uint_as_float(rr[1]); }
;     l_reg = l_reg * alpha + ps;
;     ...
;     PK4(p0, 0, pa0); PK4(p0, 8, pa1); PK4(p1, 0, pa2); PK4(p1, 8, pa3);
;     ...
; }
; DEVI void qkt(f32x16& p0, f32x16& p1, const char* Kb, const bf16x8 (&qr)[6], int r32, int hi, const f32x16& cinit) {
; #pragma unroll
;     for (int d0 = 0; d0 < 6; ++d0) { const int cb = (d0 * 16 + hi * 8) * 2;
;         const bf16x8 k0 = *(const bf16x8*)(Kb + KSWZ(r32, cb)), k1 = *(const bf16x8*)(Kb + KSWZ(32 + r32, cb));
;         p0 = __builtin_amdgcn_mfma_f32_32x32x16_bf16(k0, qr[d0], d0 == 0 ? cinit : p0, 0, 0, 0);
;         p1 = __builtin_amdgcn_mfma_f32_32x32x16_bf16(k1, qr[d0], d0 == 0 ? cinit : p1, 0, 0, 0); }
; }
.Lmy_cvp2_b:
	v_exp_f32_e32 v82, v82
	s_waitcnt lgkmcnt(1)
	v_mfma_f32_32x32x16_bf16 v[98:113], v[234:237], v[150:153], v[34:49]
	v_add_u32_e32 v126, s6, v184
	v_lshl_add_u64 v[250:251], v[120:121], 0, s[12:13]
	s_add_i32 m0, s98, 0x2000
	v_exp_f32_e32 v83, v83
	v_exp_f32_e32 v84, v84
	global_load_lds_dwordx4 v[250:251], off
	v_exp_f32_e32 v85, v85
	v_exp_f32_e32 v86, v86
	v_exp_f32_e32 v87, v87
	v_exp_f32_e32 v88, v88
	s_waitcnt lgkmcnt(0)
	v_mfma_f32_32x32x16_bf16 v[66:81], v[212:215], v[150:153], v[34:49]
	ds_read_b128 v[212:215], v126
	ds_read_b128 v[216:219], v126 offset:6144
	v_add_u32_e32 v126, s6, v185
	v_lshl_add_u64 v[250:251], v[122:123], 0, s[12:13]
	s_add_i32 m0, s98, 0x4000
	v_exp_f32_e32 v89, v89
	v_exp_f32_e32 v90, v90
	global_load_lds_dwordx4 v[250:251], off
	v_exp_f32_e32 v91, v91
	v_exp_f32_e32 v92, v92
	v_exp_f32_e32 v93, v93
	s_waitcnt lgkmcnt(1)
	v_mfma_f32_32x32x16_bf16 v[98:113], v[212:215], v[138:141], v[98:113]
	s_mov_b32 m0, s99
	v_exp_f32_e32 v94, v94
	v_exp_f32_e32 v95, v95
	v_lshl_add_u64 v[250:251], v[116:117], 0, s[40:41]
	global_load_lds_dwordx4 v[116:117], off
	s_add_i32 m0, s99, 0x2000
	v_exp_f32_e32 v96, v96
	v_exp_f32_e32 v97, v97
	v_add_u32_e32 v174, 0x2000, v203
	global_load_lds_dwordx4 v[250:251], off
	s_waitcnt lgkmcnt(0)
	v_mfma_f32_32x32x16_bf16 v[66:81], v[216:219], v[138:141], v[66:81]
	ds_read_b128 v[212:215], v126
	ds_read_b128 v[216:219], v126 offset:6144
	v_add_u32_e32 v126, s6, v205
	s_waitcnt lgkmcnt(1)
	v_mfma_f32_32x32x16_bf16 v[98:113], v[212:215], v[134:137], v[98:113]
	ds_read_b128 v[212:215], v126
	ds_read_b128 v[220:223], v126 offset:6144
	v_add_u32_e32 v126, s6, v206
	s_waitcnt lgkmcnt(2)
	v_mfma_f32_32x32x16_bf16 v[66:81], v[216:219], v[134:137], v[66:81]
	ds_read_b128 v[216:219], v126
	ds_read_b128 v[224:227], v126 offset:6144
	v_add_u32_e32 v126, s6, v207
	ds_read_b128 v[228:231], v126
	ds_read_b128 v[232:235], v126 offset:6144
	v_add_f32_e32 v126, v50, v82
	v_add_f32_e32 v127, v51, v83
	v_cvt_pk_bf16_f32 v50, v50, v51
	v_cvt_pk_bf16_f32 v51, v52, v53
	s_waitcnt lgkmcnt(5)
	v_mfma_f32_32x32x16_bf16 v[98:113], v[212:215], v[130:133], v[98:113]
	v_add_f32_e64 v212, v52, v84
	v_add_f32_e64 v213, v53, v85
	v_cvt_pk_bf16_f32 v52, v54, v55
	v_cvt_pk_bf16_f32 v53, v56, v57
	v_add_f32_e64 v126, v212, v126
	v_add_f32_e64 v127, v213, v127
	v_add_f32_e64 v212, v54, v86
	v_add_f32_e64 v213, v55, v87
	v_cvt_pk_bf16_f32 v54, v58, v59
	s_waitcnt lgkmcnt(4)
	v_mfma_f32_32x32x16_bf16 v[66:81], v[220:223], v[130:133], v[66:81]
	v_add_f32_e64 v126, v212, v126
	v_add_f32_e64 v127, v213, v127
	v_add_f32_e64 v212, v56, v88
	v_add_f32_e64 v213, v57, v89
	v_cvt_pk_bf16_f32 v55, v60, v61
	v_cvt_pk_bf16_f32 v56, v62, v63
	v_cvt_pk_bf16_f32 v57, v64, v65
	v_add_f32_e64 v126, v212, v126
	v_add_f32_e64 v127, v213, v127
	v_add_f32_e32 v212, v58, v90
	v_add_f32_e32 v213, v59, v91
	v_cvt_pk_bf16_f32 v58, v82, v83
	v_cvt_pk_bf16_f32 v59, v84, v85
	s_waitcnt lgkmcnt(3)
	v_mfma_f32_32x32x16_bf16 v[98:113], v[216:219], v[146:149], v[98:113]
	v_add_f32_e64 v126, v212, v126
	v_add_f32_e64 v127, v213, v127
	v_add_f32_e64 v212, v60, v92
	v_add_f32_e64 v213, v61, v93
	v_cvt_pk_bf16_f32 v60, v86, v87
	v_cvt_pk_bf16_f32 v61, v88, v89
	v_add_f32_e64 v126, v212, v126
	v_add_f32_e64 v127, v213, v127
	v_add_f32_e32 v212, v62, v94
	v_add_f32_e32 v213, v63, v95
	v_cvt_pk_bf16_f32 v62, v90, v91
	v_cvt_pk_bf16_f32 v63, v92, v93
	s_waitcnt lgkmcnt(2)
	v_mfma_f32_32x32x16_bf16 v[66:81], v[224:227], v[146:149], v[66:81]
	v_add_f32_e64 v126, v212, v126
	v_add_f32_e64 v127, v213, v127
	v_add_f32_e64 v212, v64, v96
	v_add_f32_e64 v213, v65, v97
	v_cvt_pk_bf16_f32 v64, v94, v95
	v_cvt_pk_bf16_f32 v65, v96, v97
	ds_read_b64_tr_b16 v[154:155], v174 offset:0
	ds_read_b64_tr_b16 v[156:157], v174 offset:0x400
	ds_read_b64_tr_b16 v[158:159], v174 offset:0x800
	ds_read_b64_tr_b16 v[160:161], v174 offset:0xc00
	ds_read_b64_tr_b16 v[162:163], v174 offset:0x1000
	ds_read_b64_tr_b16 v[164:165], v174 offset:0x1400
	ds_read_b64_tr_b16 v[166:167], v174 offset:0x1800
	ds_read_b64_tr_b16 v[168:169], v174 offset:0x1c00
	v_add_f32_e64 v126, v212, v126
	v_add_f32_e64 v127, v213, v127
	ds_read_b64_tr_b16 v[212:213], v174 offset:0x200
	ds_read_b64_tr_b16 v[214:215], v174 offset:0x600
	ds_read_b64_tr_b16 v[216:217], v174 offset:0xa00
	s_waitcnt lgkmcnt(12)
	v_mfma_f32_32x32x16_bf16 v[98:113], v[228:231], v[142:145], v[98:113]
	ds_read_b64_tr_b16 v[218:219], v174 offset:0xe00
	ds_read_b64_tr_b16 v[220:221], v174 offset:0x1200
	ds_read_b64_tr_b16 v[222:223], v174 offset:0x1600
	ds_read_b64_tr_b16 v[224:225], v174 offset:0x1a00
	ds_read_b64_tr_b16 v[226:227], v174 offset:0x1e00
	v_add_f32_e32 v126, v126, v127
	s_waitcnt lgkmcnt(15)
	v_mfma_f32_32x32x16_bf16 v[66:81], v[232:235], v[142:145], v[66:81]
	v_mov_b32_e32 v127, v126
	s_nop 1
	v_permlane32_swap_b32_e32 v126, v127
	s_waitcnt lgkmcnt(14)
	v_mfma_f32_32x32x16_bf16 v[18:33], v[50:53], v[154:157], v[18:33]
	s_waitcnt lgkmcnt(6)
	v_mfma_f32_32x32x16_bf16 v[2:17], v[50:53], v[212:215], v[2:17]
	s_nop 4
	v_max_f32_e32 v249, v99, v99
	v_max_f32_e32 v250, v98, v98
	v_max_f32_e32 v249, v250, v249
	v_max3_f32 v249, v249, v100, v101
	v_max3_f32 v249, v249, v102, v103
	v_max3_f32 v251, v249, v104, v105
	v_max3_f32 v251, v251, v106, v107
	v_exp_f32_e32 v50, v98
	v_exp_f32_e32 v51, v99
	v_exp_f32_e32 v52, v100
	v_exp_f32_e32 v53, v101
	v_mfma_f32_32x32x16_bf16 v[18:33], v[54:57], v[158:161], v[18:33]
	s_waitcnt lgkmcnt(4)
	v_mfma_f32_32x32x16_bf16 v[2:17], v[54:57], v[216:219], v[2:17]
	v_max3_f32 v251, v251, v108, v109
	v_max3_f32 v251, v251, v110, v111
	v_max3_f32 v251, v251, v112, v113
	v_max3_f32 v251, v251, v66, v67
	v_max3_f32 v251, v251, v68, v69
	v_max3_f32 v251, v251, v70, v71
	v_max3_f32 v251, v251, v72, v73
	v_exp_f32_e32 v54, v102
	v_exp_f32_e32 v55, v103
	v_exp_f32_e32 v56, v104
	v_exp_f32_e32 v57, v105
	v_mfma_f32_32x32x16_bf16 v[18:33], v[58:61], v[162:165], v[18:33]
	s_waitcnt lgkmcnt(2)
	v_mfma_f32_32x32x16_bf16 v[2:17], v[58:61], v[220:223], v[2:17]
	v_max3_f32 v251, v251, v74, v75
	v_max3_f32 v251, v251, v76, v77
	v_max3_f32 v251, v251, v78, v79
	v_max3_f32 v251, v251, v80, v81
	v_mov_b32_e32 v252, v251
	s_nop 1
	v_permlane32_swap_b32_e32 v251, v252
	v_exp_f32_e32 v58, v106
	v_exp_f32_e32 v59, v107
	v_exp_f32_e32 v60, v108
	v_exp_f32_e32 v61, v109
	v_mfma_f32_32x32x16_bf16 v[18:33], v[62:65], v[166:169], v[18:33]
	s_waitcnt lgkmcnt(0)
	v_mfma_f32_32x32x16_bf16 v[2:17], v[62:65], v[224:227], v[2:17]
	v_exp_f32_e32 v62, v110
	v_exp_f32_e32 v63, v111
	v_exp_f32_e32 v64, v112
	v_exp_f32_e32 v65, v113
	v_max_f32_e32 v252, v252, v252
	v_max_f32_e32 v251, v251, v251
	v_max_f32_e32 v174, v251, v252
	v_cmp_ge_f32_e32 vcc, s80, v174
	s_cmp_lg_u64 vcc, exec
	s_cselect_b64 s[6:7], -1, 0
	s_cbranch_scc1 .LBB0_2275
	v_mov_b32_e32 v203, 1.0
	v_mov_b32_e32 v204, v210
	s_branch .LBB0_2280

; __global__ void __launch_bounds__(512, 2) k_mega(Params p_unused) {
;     extern __shared__ __attribute__((aligned(16))) char smem[];
	.amdhsa_kernel _Z6k_mega6Params
		.amdhsa_group_segment_fixed_size 0
		.amdhsa_private_segment_fixed_size 0
		.amdhsa_kernarg_size 816
		.amdhsa_user_sgpr_count 2
		.amdhsa_user_sgpr_dispatch_ptr 0
		.amdhsa_user_sgpr_queue_ptr 0
		.amdhsa_user_sgpr_kernarg_segment_ptr 1
		.amdhsa_user_sgpr_dispatch_id 0
		.amdhsa_user_sgpr_kernarg_preload_length 0
		.amdhsa_user_sgpr_kernarg_preload_offset 0
		.amdhsa_user_sgpr_private_segment_size 0
		.amdhsa_uses_dynamic_stack 0
		.amdhsa_enable_private_segment 0
		.amdhsa_system_sgpr_workgroup_id_x 1
		.amdhsa_system_sgpr_workgroup_id_y 0
		.amdhsa_system_sgpr_workgroup_id_z 0
		.amdhsa_system_sgpr_workgroup_info 0
		.amdhsa_system_vgpr_workitem_id 0
		.amdhsa_next_free_vgpr 256
		.amdhsa_next_free_sgpr 102
		.amdhsa_accum_offset 256
		.amdhsa_reserve_vcc 1
		.amdhsa_float_round_mode_32 0
		.amdhsa_float_round_mode_16_64 0
		.amdhsa_float_denorm_mode_32 3
		.amdhsa_float_denorm_mode_16_64 3
		.amdhsa_dx10_clamp 1
		.amdhsa_ieee_mode 1
		.amdhsa_fp16_overflow 0
		.amdhsa_tg_split 0
		.amdhsa_exception_fp_ieee_invalid_op 0
		.amdhsa_exception_fp_denorm_src 0
		.amdhsa_exception_fp_ieee_div_zero 0
		.amdhsa_exception_fp_ieee_overflow 0
		.amdhsa_exception_fp_ieee_underflow 0
		.amdhsa_exception_fp_ieee_inexact 0
		.amdhsa_exception_int_div_zero 0
	.end_amdhsa_kernel

; __global__ void __launch_bounds__(512, 2) k_mega(Params p_unused) {
;     extern __shared__ __attribute__((aligned(16))) char smem[];
.Lfunc_end0:
	.size	_Z6k_mega6Params, .Lfunc_end0-_Z6k_mega6Params
	.set _Z6k_mega6Params.num_vgpr, 256
	.set _Z6k_mega6Params.num_agpr, 0
	.set _Z6k_mega6Params.numbered_sgpr, 102
	.set _Z6k_mega6Params.num_named_barrier, 0
	.set _Z6k_mega6Params.private_seg_size, 0
	.set _Z6k_mega6Params.uses_vcc, 1
	.set _Z6k_mega6Params.uses_flat_scratch, 0
	.set _Z6k_mega6Params.has_dyn_sized_stack, 0
	.set _Z6k_mega6Params.has_recursion, 0
	.set _Z6k_mega6Params.has_indirect_call, 0

; __global__ void __launch_bounds__(512, 2) k_mega(Params p_unused) {
;     extern __shared__ __attribute__((aligned(16))) char smem[];
amdhsa.kernels:
  - .agpr_count:     0
    .args:
      - .offset:         0
        .size:           560
        .value_kind:     by_value
      - .offset:         560
        .size:           4
        .value_kind:     hidden_block_count_x
      - .offset:         564
        .size:           4
        .value_kind:     hidden_block_count_y
      - .offset:         568
        .size:           4
        .value_kind:     hidden_block_count_z
      - .offset:         572
        .size:           2
        .value_kind:     hidden_group_size_x
      - .offset:         574
        .size:           2
        .value_kind:     hidden_group_size_y
      - .offset:         576
        .size:           2
        .value_kind:     hidden_group_size_z
      - .offset:         578
        .size:           2
        .value_kind:     hidden_remainder_x
      - .offset:         580
        .size:           2
        .value_kind:     hidden_remainder_y
      - .offset:         582
        .size:           2
        .value_kind:     hidden_remainder_z
      - .offset:         600
        .size:           8
        .value_kind:     hidden_global_offset_x
      - .offset:         608
        .size:           8
        .value_kind:     hidden_global_offset_y
      - .offset:         616
        .size:           8
        .value_kind:     hidden_global_offset_z
      - .offset:         624
        .size:           2
        .value_kind:     hidden_grid_dims
      - .offset:         680
        .size:           4
        .value_kind:     hidden_dynamic_lds_size
    .group_segment_fixed_size: 0
    .kernarg_segment_align: 8
    .kernarg_segment_size: 816
    .language:       OpenCL C
    .language_version:
      - 2
      - 0
    .max_flat_workgroup_size: 512
    .name:           _Z6k_mega6Params
    .private_segment_fixed_size: 0
    .sgpr_count:     108
    .sgpr_spill_count: 9
    .symbol:         _Z6k_mega6Params.kd
    .uniform_work_group_size: 1
    .uses_dynamic_stack: false
    .vgpr_count:     256
    .vgpr_spill_count: 0
    .wavefront_size: 64
